# v33 (P6 streamer tail: in-place carry + packed multiply) with an unexecuted 4-byte pad after P6 so the later loop heads keep v29's byte phase (matched-placement test)
# speedup vs baseline: 1.0004x; 1.0004x over previous
.LBB0_934:
	s_ashr_i32 s3, s97, 31
	s_lshr_b32 s3, s3, 26
	s_add_i32 s3, s97, s3
	s_and_b32 s3, s3, 0xffffc0
	s_sub_i32 s3, s97, s3
	s_lshl_b32 s3, s3, 8
	v_readlane_b32 s4, v249, 5
	s_add_i32 s3, s3, s4
	s_nop 15
	s_nop 15
	v_mbcnt_lo_u32_b32 v0, -1, 0
	v_mbcnt_hi_u32_b32 v0, -1, v0
	s_nop 0
	v_and_or_b32 v36, v0, 15, s3
	s_lshl_b32 s3, s96, 8
	v_and_b32_e32 v0, -16, v0
	s_or_b32 s3, s3, s88
	v_add_u32_e32 v32, s3, v0
	v_ashrrev_i32_e32 v33, 31, v32
	v_lshlrev_b64 v[34:35], 1, v[32:33]
	v_ashrrev_i32_e32 v37, 31, v36
	v_or_b32_e32 v40, 16, v36
	v_lshl_add_u64 v[38:39], s[44:45], 0, v[34:35]
	v_lshlrev_b64 v[192:193], 13, v[36:37]
	v_ashrrev_i32_e32 v41, 31, v40
	v_or_b32_e32 v44, 32, v36
	v_or_b32_e32 v196, 48, v36
	v_lshl_add_u64 v[12:13], v[32:33], 2, s[50:51]
	v_lshl_add_u64 v[16:17], v[38:39], 0, v[192:193]
	v_lshlrev_b64 v[194:195], 13, v[40:41]
	v_ashrrev_i32_e32 v45, 31, v44
	v_ashrrev_i32_e32 v197, 31, v196
	global_load_dwordx4 v[0:3], v[12:13], off offset:48
	global_load_dwordx4 v[4:7], v[12:13], off offset:32
	global_load_dwordx4 v[8:11], v[12:13], off offset:16
	s_nop 0
	global_load_dwordx4 v[12:15], v[12:13], off
	s_nop 0
	global_load_dwordx4 v[48:51], v[16:17], off offset:16
	global_load_dwordx4 v[52:55], v[16:17], off
	v_lshl_add_u64 v[16:17], v[38:39], 0, v[194:195]
	v_lshlrev_b64 v[46:47], 13, v[44:45]
	v_lshlrev_b64 v[42:43], 13, v[196:197]
	global_load_dwordx4 v[56:59], v[16:17], off offset:16
	global_load_dwordx4 v[60:63], v[16:17], off
	v_lshl_add_u64 v[16:17], v[38:39], 0, v[46:47]
	v_lshl_add_u64 v[20:21], v[38:39], 0, v[42:43]
	global_load_dwordx4 v[24:27], v[16:17], off offset:16
	global_load_dwordx4 v[28:31], v[16:17], off
	s_nop 0
	global_load_dwordx4 v[16:19], v[20:21], off offset:16
	s_nop 0
	global_load_dwordx4 v[20:23], v[20:21], off
	v_lshl_add_u64 v[34:35], s[40:41], 0, v[34:35]
	v_lshlrev_b64 v[198:199], 12, v[36:37]
	v_lshlrev_b64 v[222:223], 12, v[40:41]
	v_lshlrev_b64 v[44:45], 12, v[44:45]
	v_lshlrev_b64 v[40:41], 12, v[196:197]
	s_waitcnt vmcnt(6)
	v_lshlrev_b32_e32 v196, 16, v52
	v_and_b32_e32 v197, 0xffff0000, v52
	v_lshlrev_b32_e32 v52, 16, v53
	v_and_b32_e32 v53, 0xffff0000, v53
	v_pk_fma_f32 v[224:225], v[190:191], s[46:47], v[52:53] op_sel_hi:[1,0,1]
	v_lshlrev_b32_e32 v52, 16, v54
	v_and_b32_e32 v53, 0xffff0000, v54
	v_lshlrev_b32_e32 v54, 16, v55
	v_and_b32_e32 v55, 0xffff0000, v55
	v_pk_fma_f32 v[196:197], v[188:189], s[46:47], v[196:197] op_sel_hi:[1,0,1]
	v_pk_fma_f32 v[226:227], v[186:187], s[46:47], v[54:55] op_sel_hi:[1,0,1]
	v_pk_fma_f32 v[228:229], v[184:185], s[46:47], v[52:53] op_sel_hi:[1,0,1]
	v_cvt_pk_bf16_f32 v52, v196, v197
	v_cvt_pk_bf16_f32 v55, v226, v227
	v_lshl_add_u64 v[192:193], v[34:35], 0, v[192:193]
	v_cvt_pk_bf16_f32 v54, v228, v229
	v_cvt_pk_bf16_f32 v53, v224, v225
	global_store_dwordx4 v[192:193], v[52:55], off
	v_lshl_add_u64 v[46:47], v[34:35], 0, v[46:47]
	v_lshl_add_u64 v[42:43], v[34:35], 0, v[42:43]
	v_pk_mul_f32 v[54:55], v[12:13], v[196:197]
	v_mov_b32_e32 v52, v203
	v_pk_mul_f32 v[196:197], v[8:9], v[228:229]
	v_cvt_pk_fp8_f32 v52, v54, v55
	v_mov_b32_e32 v53, v203
	v_cvt_pk_fp8_f32 v53, v196, v197
	v_pk_mul_f32 v[54:55], v[14:15], v[224:225]
	v_pk_mul_f32 v[196:197], v[10:11], v[226:227]
	v_cvt_pk_fp8_f32 v52, v54, v55 op_sel:[0,0,1]
	v_lshlrev_b32_e32 v54, 16, v48
	v_and_b32_e32 v55, 0xffff0000, v48
	v_lshlrev_b32_e32 v48, 16, v49
	v_and_b32_e32 v49, 0xffff0000, v49
	v_cvt_pk_fp8_f32 v53, v196, v197 op_sel:[0,0,1]
	v_pk_fma_f32 v[196:197], v[158:159], s[46:47], v[48:49] op_sel_hi:[1,0,1]
	v_lshlrev_b32_e32 v48, 16, v50
	v_and_b32_e32 v49, 0xffff0000, v50
	v_pk_fma_f32 v[54:55], v[156:157], s[46:47], v[54:55] op_sel_hi:[1,0,1]
	v_lshlrev_b32_e32 v50, 16, v51
	v_and_b32_e32 v51, 0xffff0000, v51
	v_pk_fma_f32 v[226:227], v[152:153], s[46:47], v[48:49] op_sel_hi:[1,0,1]
	v_pk_fma_f32 v[224:225], v[154:155], s[46:47], v[50:51] op_sel_hi:[1,0,1]
	v_cvt_pk_bf16_f32 v48, v54, v55
	v_cvt_pk_bf16_f32 v50, v226, v227
	v_pk_mul_f32 v[228:229], v[4:5], v[54:55]
	v_pk_mul_f32 v[226:227], v[0:1], v[226:227]
	v_mov_b32_e32 v54, v203
	v_mov_b32_e32 v55, v203
	v_cvt_pk_fp8_f32 v54, v228, v229
	v_cvt_pk_fp8_f32 v55, v226, v227
	v_cvt_pk_bf16_f32 v49, v196, v197
	v_cvt_pk_bf16_f32 v51, v224, v225
	v_pk_mul_f32 v[196:197], v[6:7], v[196:197]
	v_pk_mul_f32 v[224:225], v[2:3], v[224:225]
	v_cvt_pk_fp8_f32 v54, v196, v197 op_sel:[0,0,1]
	v_cvt_pk_fp8_f32 v55, v224, v225 op_sel:[0,0,1]
	global_store_dwordx4 v[192:193], v[48:51], off offset:16
	v_lshl_add_u64 v[192:193], v[34:35], 0, v[194:195]
	s_nop 0
	v_lshl_add_u64 v[48:49], s[42:43], 0, v[198:199]
	v_lshl_add_u64 v[48:49], v[48:49], 0, v[32:33]
	global_store_dwordx4 v[48:49], v[52:55], off
	s_waitcnt vmcnt(7)
	v_lshlrev_b32_e32 v48, 16, v60
	v_and_b32_e32 v49, 0xffff0000, v60
	v_lshlrev_b32_e32 v50, 16, v61
	v_and_b32_e32 v51, 0xffff0000, v61
	v_pk_fma_f32 v[52:53], v[182:183], s[46:47], v[50:51] op_sel_hi:[1,0,1]
	v_pk_fma_f32 v[54:55], v[180:181], s[46:47], v[48:49] op_sel_hi:[1,0,1]
	v_lshlrev_b32_e32 v48, 16, v62
	v_and_b32_e32 v49, 0xffff0000, v62
	v_lshlrev_b32_e32 v50, 16, v63
	v_and_b32_e32 v51, 0xffff0000, v63
	v_pk_fma_f32 v[60:61], v[178:179], s[46:47], v[50:51] op_sel_hi:[1,0,1]
	v_pk_fma_f32 v[62:63], v[176:177], s[46:47], v[48:49] op_sel_hi:[1,0,1]
	v_cvt_pk_bf16_f32 v49, v52, v53
	v_cvt_pk_bf16_f32 v51, v60, v61
	v_cvt_pk_bf16_f32 v48, v54, v55
	s_nop 0
	v_cvt_pk_bf16_f32 v50, v62, v63
	global_store_dwordx4 v[192:193], v[48:51], off
	s_nop 1
	v_pk_mul_f32 v[50:51], v[12:13], v[54:55]
	v_pk_mul_f32 v[54:55], v[8:9], v[62:63]
	v_mov_b32_e32 v49, v203
	v_mov_b32_e32 v48, v203
	v_cvt_pk_fp8_f32 v49, v54, v55
	v_cvt_pk_fp8_f32 v48, v50, v51
	v_pk_mul_f32 v[50:51], v[14:15], v[52:53]
	v_pk_mul_f32 v[52:53], v[10:11], v[60:61]
	v_lshlrev_b32_e32 v54, 16, v59
	v_cvt_pk_fp8_f32 v49, v52, v53 op_sel:[0,0,1]
	v_lshlrev_b32_e32 v52, 16, v57
	v_and_b32_e32 v53, 0xffff0000, v57
	v_cvt_pk_fp8_f32 v48, v50, v51 op_sel:[0,0,1]
	v_lshlrev_b32_e32 v50, 16, v56
	v_and_b32_e32 v51, 0xffff0000, v56
	v_pk_fma_f32 v[56:57], v[150:151], s[46:47], v[52:53] op_sel_hi:[1,0,1]
	v_lshlrev_b32_e32 v52, 16, v58
	v_and_b32_e32 v53, 0xffff0000, v58
	v_pk_fma_f32 v[50:51], v[148:149], s[46:47], v[50:51] op_sel_hi:[1,0,1]
	v_and_b32_e32 v55, 0xffff0000, v59
	v_pk_fma_f32 v[60:61], v[144:145], s[46:47], v[52:53] op_sel_hi:[1,0,1]
	v_pk_fma_f32 v[58:59], v[146:147], s[46:47], v[54:55] op_sel_hi:[1,0,1]
	v_cvt_pk_bf16_f32 v52, v50, v51
	v_cvt_pk_bf16_f32 v54, v60, v61
	v_pk_mul_f32 v[62:63], v[4:5], v[50:51]
	v_pk_mul_f32 v[60:61], v[0:1], v[60:61]
	v_mov_b32_e32 v50, v203
	v_mov_b32_e32 v51, v203
	v_cvt_pk_fp8_f32 v50, v62, v63
	v_cvt_pk_fp8_f32 v51, v60, v61
	v_cvt_pk_bf16_f32 v53, v56, v57
	v_cvt_pk_bf16_f32 v55, v58, v59
	v_pk_mul_f32 v[56:57], v[6:7], v[56:57]
	v_pk_mul_f32 v[58:59], v[2:3], v[58:59]
	v_cvt_pk_fp8_f32 v50, v56, v57 op_sel:[0,0,1]
	v_cvt_pk_fp8_f32 v51, v58, v59 op_sel:[0,0,1]
	global_store_dwordx4 v[192:193], v[52:55], off offset:16
	s_nop 1
	v_lshl_add_u64 v[52:53], s[42:43], 0, v[222:223]
	v_lshl_add_u64 v[52:53], v[52:53], 0, v[32:33]
	global_store_dwordx4 v[52:53], v[48:51], off
	s_waitcnt vmcnt(8)
	s_nop 0
	v_lshlrev_b32_e32 v48, 16, v28
	v_and_b32_e32 v49, 0xffff0000, v28
	v_lshlrev_b32_e32 v28, 16, v29
	v_and_b32_e32 v29, 0xffff0000, v29
	v_pk_fma_f32 v[50:51], v[174:175], s[46:47], v[28:29] op_sel_hi:[1,0,1]
	v_lshlrev_b32_e32 v28, 16, v30
	v_and_b32_e32 v29, 0xffff0000, v30
	v_lshlrev_b32_e32 v30, 16, v31
	v_and_b32_e32 v31, 0xffff0000, v31
	v_pk_fma_f32 v[48:49], v[172:173], s[46:47], v[48:49] op_sel_hi:[1,0,1]
	v_pk_fma_f32 v[52:53], v[170:171], s[46:47], v[30:31] op_sel_hi:[1,0,1]
	v_pk_fma_f32 v[54:55], v[168:169], s[46:47], v[28:29] op_sel_hi:[1,0,1]
	v_cvt_pk_bf16_f32 v28, v48, v49
	v_cvt_pk_bf16_f32 v31, v52, v53
	v_cvt_pk_bf16_f32 v29, v50, v51
	s_nop 0
	v_cvt_pk_bf16_f32 v30, v54, v55
	global_store_dwordx4 v[46:47], v[28:31], off
	s_nop 1
	v_pk_mul_f32 v[30:31], v[12:13], v[48:49]
	v_mov_b32_e32 v28, v203
	v_pk_mul_f32 v[48:49], v[8:9], v[54:55]
	v_cvt_pk_fp8_f32 v28, v30, v31
	v_mov_b32_e32 v29, v203
	v_cvt_pk_fp8_f32 v29, v48, v49
	v_pk_mul_f32 v[30:31], v[14:15], v[50:51]
	v_pk_mul_f32 v[48:49], v[10:11], v[52:53]
	v_cvt_pk_fp8_f32 v28, v30, v31 op_sel:[0,0,1]
	v_lshlrev_b32_e32 v30, 16, v24
	v_and_b32_e32 v31, 0xffff0000, v24
	v_lshlrev_b32_e32 v24, 16, v25
	v_and_b32_e32 v25, 0xffff0000, v25
	v_cvt_pk_fp8_f32 v29, v48, v49 op_sel:[0,0,1]
	v_pk_fma_f32 v[48:49], v[142:143], s[46:47], v[24:25] op_sel_hi:[1,0,1]
	v_lshlrev_b32_e32 v24, 16, v26
	v_and_b32_e32 v25, 0xffff0000, v26
	v_pk_fma_f32 v[30:31], v[140:141], s[46:47], v[30:31] op_sel_hi:[1,0,1]
	v_lshlrev_b32_e32 v26, 16, v27
	v_and_b32_e32 v27, 0xffff0000, v27
	v_pk_fma_f32 v[52:53], v[136:137], s[46:47], v[24:25] op_sel_hi:[1,0,1]
	v_pk_fma_f32 v[50:51], v[138:139], s[46:47], v[26:27] op_sel_hi:[1,0,1]
	v_cvt_pk_bf16_f32 v24, v30, v31
	v_cvt_pk_bf16_f32 v26, v52, v53
	v_pk_mul_f32 v[54:55], v[4:5], v[30:31]
	v_pk_mul_f32 v[52:53], v[0:1], v[52:53]
	v_mov_b32_e32 v30, v203
	v_mov_b32_e32 v31, v203
	v_cvt_pk_fp8_f32 v30, v54, v55
	v_cvt_pk_fp8_f32 v31, v52, v53
	v_cvt_pk_bf16_f32 v25, v48, v49
	v_cvt_pk_bf16_f32 v27, v50, v51
	v_pk_mul_f32 v[48:49], v[6:7], v[48:49]
	v_pk_mul_f32 v[50:51], v[2:3], v[50:51]
	v_cvt_pk_fp8_f32 v30, v48, v49 op_sel:[0,0,1]
	v_cvt_pk_fp8_f32 v31, v50, v51 op_sel:[0,0,1]
	global_store_dwordx4 v[46:47], v[24:27], off offset:16
	s_nop 1
	v_lshl_add_u64 v[24:25], s[42:43], 0, v[44:45]
	v_lshl_add_u64 v[24:25], v[24:25], 0, v[32:33]
	global_store_dwordx4 v[24:25], v[28:31], off
	s_waitcnt vmcnt(9)
	v_lshlrev_b32_e32 v24, 16, v20
	v_and_b32_e32 v25, 0xffff0000, v20
	v_lshlrev_b32_e32 v20, 16, v21
	v_and_b32_e32 v21, 0xffff0000, v21
	v_pk_fma_f32 v[26:27], v[166:167], s[46:47], v[20:21] op_sel_hi:[1,0,1]
	v_lshlrev_b32_e32 v20, 16, v22
	v_and_b32_e32 v21, 0xffff0000, v22
	v_lshlrev_b32_e32 v22, 16, v23
	v_and_b32_e32 v23, 0xffff0000, v23
	v_pk_fma_f32 v[24:25], v[164:165], s[46:47], v[24:25] op_sel_hi:[1,0,1]
	v_pk_fma_f32 v[28:29], v[162:163], s[46:47], v[22:23] op_sel_hi:[1,0,1]
	v_pk_fma_f32 v[30:31], v[160:161], s[46:47], v[20:21] op_sel_hi:[1,0,1]
	v_cvt_pk_bf16_f32 v20, v24, v25
	v_cvt_pk_bf16_f32 v23, v28, v29
	v_cvt_pk_bf16_f32 v21, v26, v27
	s_nop 0
	v_cvt_pk_bf16_f32 v22, v30, v31
	global_store_dwordx4 v[42:43], v[20:23], off
	s_nop 1
	v_pk_mul_f32 v[22:23], v[12:13], v[24:25]
	v_mov_b32_e32 v20, v203
	v_pk_mul_f32 v[24:25], v[8:9], v[30:31]
	v_cvt_pk_fp8_f32 v20, v22, v23
	v_mov_b32_e32 v21, v203
	v_cvt_pk_fp8_f32 v21, v24, v25
	v_pk_mul_f32 v[22:23], v[14:15], v[26:27]
	v_pk_mul_f32 v[24:25], v[10:11], v[28:29]
	v_cvt_pk_fp8_f32 v20, v22, v23 op_sel:[0,0,1]
	v_lshlrev_b32_e32 v22, 16, v16
	v_and_b32_e32 v23, 0xffff0000, v16
	v_lshlrev_b32_e32 v16, 16, v17
	v_and_b32_e32 v17, 0xffff0000, v17
	v_cvt_pk_fp8_f32 v21, v24, v25 op_sel:[0,0,1]
	v_pk_fma_f32 v[24:25], v[134:135], s[46:47], v[16:17] op_sel_hi:[1,0,1]
	v_lshlrev_b32_e32 v16, 16, v18
	v_and_b32_e32 v17, 0xffff0000, v18
	v_pk_fma_f32 v[22:23], v[132:133], s[46:47], v[22:23] op_sel_hi:[1,0,1]
	v_lshlrev_b32_e32 v18, 16, v19
	v_and_b32_e32 v19, 0xffff0000, v19
	v_pk_fma_f32 v[28:29], v[128:129], s[46:47], v[16:17] op_sel_hi:[1,0,1]
	v_pk_fma_f32 v[26:27], v[130:131], s[46:47], v[18:19] op_sel_hi:[1,0,1]
	v_cvt_pk_bf16_f32 v16, v22, v23
	v_cvt_pk_bf16_f32 v18, v28, v29
	v_pk_mul_f32 v[30:31], v[4:5], v[22:23]
	v_pk_mul_f32 v[28:29], v[0:1], v[28:29]
	v_mov_b32_e32 v22, v203
	v_mov_b32_e32 v23, v203
	v_cvt_pk_fp8_f32 v22, v30, v31
	v_cvt_pk_fp8_f32 v23, v28, v29
	v_cvt_pk_bf16_f32 v17, v24, v25
	v_cvt_pk_bf16_f32 v19, v26, v27
	v_pk_mul_f32 v[24:25], v[6:7], v[24:25]
	v_pk_mul_f32 v[26:27], v[2:3], v[26:27]
	v_cvt_pk_fp8_f32 v22, v24, v25 op_sel:[0,0,1]
	v_cvt_pk_fp8_f32 v23, v26, v27 op_sel:[0,0,1]
	global_store_dwordx4 v[42:43], v[16:19], off offset:16
	s_nop 1
	v_lshl_add_u64 v[16:17], s[42:43], 0, v[40:41]
	v_lshl_add_u64 v[16:17], v[16:17], 0, v[32:33]
	global_store_dwordx4 v[16:17], v[20:23], off
	v_add_u32_e32 v60, 0x80, v36
	v_ashrrev_i32_e32 v61, 31, v60
	v_add_u32_e32 v192, 0x90, v36
	v_lshlrev_b64 v[62:63], 13, v[60:61]
	v_ashrrev_i32_e32 v193, 31, v192
	v_add_u32_e32 v196, 0xa0, v36
	v_add_u32_e32 v36, 0xb0, v36
	v_lshl_add_u64 v[16:17], v[38:39], 0, v[62:63]
	v_lshlrev_b64 v[194:195], 13, v[192:193]
	v_ashrrev_i32_e32 v197, 31, v196
	v_ashrrev_i32_e32 v37, 31, v36
	global_load_dwordx4 v[44:47], v[16:17], off offset:16
	global_load_dwordx4 v[48:51], v[16:17], off
	v_lshl_add_u64 v[16:17], v[38:39], 0, v[194:195]
	v_lshlrev_b64 v[42:43], 13, v[196:197]
	v_lshlrev_b64 v[40:41], 13, v[36:37]
	global_load_dwordx4 v[52:55], v[16:17], off offset:16
	global_load_dwordx4 v[56:59], v[16:17], off
	v_lshl_add_u64 v[16:17], v[38:39], 0, v[42:43]
	v_lshl_add_u64 v[20:21], v[38:39], 0, v[40:41]
	global_load_dwordx4 v[24:27], v[16:17], off offset:16
	global_load_dwordx4 v[28:31], v[16:17], off
	s_nop 0
	global_load_dwordx4 v[16:19], v[20:21], off offset:16
	s_nop 0
	global_load_dwordx4 v[20:23], v[20:21], off
	v_lshlrev_b64 v[60:61], 12, v[60:61]
	v_lshlrev_b64 v[192:193], 12, v[192:193]
	v_lshlrev_b64 v[38:39], 12, v[196:197]
	v_lshlrev_b64 v[36:37], 12, v[36:37]
	s_waitcnt vmcnt(6)
	v_lshlrev_b32_e32 v196, 16, v48
	v_and_b32_e32 v197, 0xffff0000, v48
	v_lshlrev_b32_e32 v48, 16, v49
	v_and_b32_e32 v49, 0xffff0000, v49
	v_pk_fma_f32 v[198:199], v[126:127], s[46:47], v[48:49] op_sel_hi:[1,0,1]
	v_lshlrev_b32_e32 v48, 16, v50
	v_and_b32_e32 v49, 0xffff0000, v50
	v_lshlrev_b32_e32 v50, 16, v51
	v_and_b32_e32 v51, 0xffff0000, v51
	v_pk_fma_f32 v[196:197], v[124:125], s[46:47], v[196:197] op_sel_hi:[1,0,1]
	v_pk_fma_f32 v[222:223], v[122:123], s[46:47], v[50:51] op_sel_hi:[1,0,1]
	v_pk_fma_f32 v[224:225], v[120:121], s[46:47], v[48:49] op_sel_hi:[1,0,1]
	v_cvt_pk_bf16_f32 v48, v196, v197
	v_cvt_pk_bf16_f32 v51, v222, v223
	v_lshl_add_u64 v[62:63], v[34:35], 0, v[62:63]
	v_cvt_pk_bf16_f32 v50, v224, v225
	v_cvt_pk_bf16_f32 v49, v198, v199
	global_store_dwordx4 v[62:63], v[48:51], off
	v_lshl_add_u64 v[42:43], v[34:35], 0, v[42:43]
	s_nop 0
	v_pk_mul_f32 v[50:51], v[12:13], v[196:197]
	v_mov_b32_e32 v48, v203
	v_pk_mul_f32 v[196:197], v[8:9], v[224:225]
	v_cvt_pk_fp8_f32 v48, v50, v51
	v_mov_b32_e32 v49, v203
	v_cvt_pk_fp8_f32 v49, v196, v197
	v_pk_mul_f32 v[50:51], v[14:15], v[198:199]
	v_pk_mul_f32 v[196:197], v[10:11], v[222:223]
	v_cvt_pk_fp8_f32 v48, v50, v51 op_sel:[0,0,1]
	v_lshlrev_b32_e32 v50, 16, v44
	v_and_b32_e32 v51, 0xffff0000, v44
	v_lshlrev_b32_e32 v44, 16, v45
	v_and_b32_e32 v45, 0xffff0000, v45
	v_cvt_pk_fp8_f32 v49, v196, v197 op_sel:[0,0,1]
	v_pk_fma_f32 v[196:197], v[94:95], s[46:47], v[44:45] op_sel_hi:[1,0,1]
	v_lshlrev_b32_e32 v44, 16, v46
	v_and_b32_e32 v45, 0xffff0000, v46
	v_pk_fma_f32 v[50:51], v[92:93], s[46:47], v[50:51] op_sel_hi:[1,0,1]
	v_lshlrev_b32_e32 v46, 16, v47
	v_and_b32_e32 v47, 0xffff0000, v47
	v_pk_fma_f32 v[222:223], v[88:89], s[46:47], v[44:45] op_sel_hi:[1,0,1]
	v_pk_fma_f32 v[198:199], v[90:91], s[46:47], v[46:47] op_sel_hi:[1,0,1]
	v_cvt_pk_bf16_f32 v44, v50, v51
	v_cvt_pk_bf16_f32 v46, v222, v223
	v_pk_mul_f32 v[224:225], v[4:5], v[50:51]
	v_pk_mul_f32 v[222:223], v[0:1], v[222:223]
	v_mov_b32_e32 v50, v203
	v_mov_b32_e32 v51, v203
	v_cvt_pk_fp8_f32 v50, v224, v225
	v_cvt_pk_fp8_f32 v51, v222, v223
	v_cvt_pk_bf16_f32 v45, v196, v197
	v_cvt_pk_bf16_f32 v47, v198, v199
	v_pk_mul_f32 v[196:197], v[6:7], v[196:197]
	v_pk_mul_f32 v[198:199], v[2:3], v[198:199]
	v_cvt_pk_fp8_f32 v50, v196, v197 op_sel:[0,0,1]
	v_cvt_pk_fp8_f32 v51, v198, v199 op_sel:[0,0,1]
	global_store_dwordx4 v[62:63], v[44:47], off offset:16
	s_nop 1
	v_lshl_add_u64 v[44:45], s[42:43], 0, v[60:61]
	v_lshl_add_u64 v[44:45], v[44:45], 0, v[32:33]
	global_store_dwordx4 v[44:45], v[48:51], off
	s_waitcnt vmcnt(7)
	v_lshlrev_b32_e32 v44, 16, v56
	v_and_b32_e32 v45, 0xffff0000, v56
	v_lshlrev_b32_e32 v46, 16, v57
	v_and_b32_e32 v47, 0xffff0000, v57
	v_pk_fma_f32 v[48:49], v[118:119], s[46:47], v[46:47] op_sel_hi:[1,0,1]
	v_pk_fma_f32 v[50:51], v[116:117], s[46:47], v[44:45] op_sel_hi:[1,0,1]
	v_lshlrev_b32_e32 v44, 16, v58
	v_and_b32_e32 v45, 0xffff0000, v58
	v_lshlrev_b32_e32 v46, 16, v59
	v_and_b32_e32 v47, 0xffff0000, v59
	v_pk_fma_f32 v[56:57], v[114:115], s[46:47], v[46:47] op_sel_hi:[1,0,1]
	v_pk_fma_f32 v[58:59], v[112:113], s[46:47], v[44:45] op_sel_hi:[1,0,1]
	v_cvt_pk_bf16_f32 v45, v48, v49
	v_cvt_pk_bf16_f32 v47, v56, v57
	v_lshl_add_u64 v[60:61], v[34:35], 0, v[194:195]
	v_cvt_pk_bf16_f32 v46, v58, v59
	v_cvt_pk_bf16_f32 v44, v50, v51
	global_store_dwordx4 v[60:61], v[44:47], off
	v_lshl_add_u64 v[34:35], v[34:35], 0, v[40:41]
	s_nop 0
	v_pk_mul_f32 v[46:47], v[12:13], v[50:51]
	v_pk_mul_f32 v[50:51], v[8:9], v[58:59]
	v_mov_b32_e32 v45, v203
	v_mov_b32_e32 v44, v203
	v_cvt_pk_fp8_f32 v45, v50, v51
	v_cvt_pk_fp8_f32 v44, v46, v47
	v_pk_mul_f32 v[46:47], v[14:15], v[48:49]
	v_pk_mul_f32 v[48:49], v[10:11], v[56:57]
	v_lshlrev_b32_e32 v50, 16, v55
	v_cvt_pk_fp8_f32 v45, v48, v49 op_sel:[0,0,1]
	v_lshlrev_b32_e32 v48, 16, v53
	v_and_b32_e32 v49, 0xffff0000, v53
	v_cvt_pk_fp8_f32 v44, v46, v47 op_sel:[0,0,1]
	v_lshlrev_b32_e32 v46, 16, v52
	v_and_b32_e32 v47, 0xffff0000, v52
	v_pk_fma_f32 v[52:53], v[86:87], s[46:47], v[48:49] op_sel_hi:[1,0,1]
	v_lshlrev_b32_e32 v48, 16, v54
	v_and_b32_e32 v49, 0xffff0000, v54
	v_pk_fma_f32 v[46:47], v[84:85], s[46:47], v[46:47] op_sel_hi:[1,0,1]
	v_and_b32_e32 v51, 0xffff0000, v55
	v_pk_fma_f32 v[56:57], v[80:81], s[46:47], v[48:49] op_sel_hi:[1,0,1]
	v_pk_fma_f32 v[54:55], v[82:83], s[46:47], v[50:51] op_sel_hi:[1,0,1]
	v_cvt_pk_bf16_f32 v48, v46, v47
	v_cvt_pk_bf16_f32 v50, v56, v57
	v_pk_mul_f32 v[58:59], v[4:5], v[46:47]
	v_pk_mul_f32 v[56:57], v[0:1], v[56:57]
	v_mov_b32_e32 v46, v203
	v_mov_b32_e32 v47, v203
	v_cvt_pk_fp8_f32 v46, v58, v59
	v_cvt_pk_fp8_f32 v47, v56, v57
	v_cvt_pk_bf16_f32 v49, v52, v53
	v_cvt_pk_bf16_f32 v51, v54, v55
	v_pk_mul_f32 v[52:53], v[6:7], v[52:53]
	v_pk_mul_f32 v[54:55], v[2:3], v[54:55]
	v_cvt_pk_fp8_f32 v46, v52, v53 op_sel:[0,0,1]
	v_cvt_pk_fp8_f32 v47, v54, v55 op_sel:[0,0,1]
	global_store_dwordx4 v[60:61], v[48:51], off offset:16
	s_nop 1
	v_lshl_add_u64 v[48:49], s[42:43], 0, v[192:193]
	v_lshl_add_u64 v[48:49], v[48:49], 0, v[32:33]
	global_store_dwordx4 v[48:49], v[44:47], off
	s_waitcnt vmcnt(8)
	s_nop 0
	v_lshlrev_b32_e32 v44, 16, v28
	v_and_b32_e32 v45, 0xffff0000, v28
	v_lshlrev_b32_e32 v28, 16, v29
	v_and_b32_e32 v29, 0xffff0000, v29
	v_pk_fma_f32 v[46:47], v[110:111], s[46:47], v[28:29] op_sel_hi:[1,0,1]
	v_lshlrev_b32_e32 v28, 16, v30
	v_and_b32_e32 v29, 0xffff0000, v30
	v_lshlrev_b32_e32 v30, 16, v31
	v_and_b32_e32 v31, 0xffff0000, v31
	v_pk_fma_f32 v[44:45], v[108:109], s[46:47], v[44:45] op_sel_hi:[1,0,1]
	v_pk_fma_f32 v[48:49], v[106:107], s[46:47], v[30:31] op_sel_hi:[1,0,1]
	v_pk_fma_f32 v[50:51], v[104:105], s[46:47], v[28:29] op_sel_hi:[1,0,1]
	v_cvt_pk_bf16_f32 v28, v44, v45
	v_cvt_pk_bf16_f32 v31, v48, v49
	v_cvt_pk_bf16_f32 v29, v46, v47
	s_nop 0
	v_cvt_pk_bf16_f32 v30, v50, v51
	global_store_dwordx4 v[42:43], v[28:31], off
	s_nop 1
	v_pk_mul_f32 v[30:31], v[12:13], v[44:45]
	v_mov_b32_e32 v28, v203
	v_pk_mul_f32 v[44:45], v[8:9], v[50:51]
	v_cvt_pk_fp8_f32 v28, v30, v31
	v_mov_b32_e32 v29, v203
	v_cvt_pk_fp8_f32 v29, v44, v45
	v_pk_mul_f32 v[30:31], v[14:15], v[46:47]
	v_pk_mul_f32 v[44:45], v[10:11], v[48:49]
	v_cvt_pk_fp8_f32 v28, v30, v31 op_sel:[0,0,1]
	v_lshlrev_b32_e32 v30, 16, v24
	v_and_b32_e32 v31, 0xffff0000, v24
	v_lshlrev_b32_e32 v24, 16, v25
	v_and_b32_e32 v25, 0xffff0000, v25
	v_cvt_pk_fp8_f32 v29, v44, v45 op_sel:[0,0,1]
	v_pk_fma_f32 v[44:45], v[78:79], s[46:47], v[24:25] op_sel_hi:[1,0,1]
	v_lshlrev_b32_e32 v24, 16, v26
	v_and_b32_e32 v25, 0xffff0000, v26
	v_pk_fma_f32 v[30:31], v[76:77], s[46:47], v[30:31] op_sel_hi:[1,0,1]
	v_lshlrev_b32_e32 v26, 16, v27
	v_and_b32_e32 v27, 0xffff0000, v27
	v_pk_fma_f32 v[48:49], v[72:73], s[46:47], v[24:25] op_sel_hi:[1,0,1]
	v_pk_fma_f32 v[46:47], v[74:75], s[46:47], v[26:27] op_sel_hi:[1,0,1]
	v_cvt_pk_bf16_f32 v24, v30, v31
	v_cvt_pk_bf16_f32 v26, v48, v49
	v_pk_mul_f32 v[50:51], v[4:5], v[30:31]
	v_pk_mul_f32 v[48:49], v[0:1], v[48:49]
	v_mov_b32_e32 v30, v203
	v_mov_b32_e32 v31, v203
	v_cvt_pk_fp8_f32 v30, v50, v51
	v_cvt_pk_fp8_f32 v31, v48, v49
	v_cvt_pk_bf16_f32 v25, v44, v45
	v_cvt_pk_bf16_f32 v27, v46, v47
	v_pk_mul_f32 v[44:45], v[6:7], v[44:45]
	v_pk_mul_f32 v[46:47], v[2:3], v[46:47]
	v_cvt_pk_fp8_f32 v30, v44, v45 op_sel:[0,0,1]
	v_cvt_pk_fp8_f32 v31, v46, v47 op_sel:[0,0,1]
	global_store_dwordx4 v[42:43], v[24:27], off offset:16
	s_nop 1
	v_lshl_add_u64 v[24:25], s[42:43], 0, v[38:39]
	v_lshl_add_u64 v[24:25], v[24:25], 0, v[32:33]
	global_store_dwordx4 v[24:25], v[28:31], off
	s_waitcnt vmcnt(9)
	v_lshlrev_b32_e32 v24, 16, v20
	v_and_b32_e32 v25, 0xffff0000, v20
	v_lshlrev_b32_e32 v20, 16, v21
	v_and_b32_e32 v21, 0xffff0000, v21
	v_pk_fma_f32 v[26:27], v[102:103], s[46:47], v[20:21] op_sel_hi:[1,0,1]
	v_lshlrev_b32_e32 v20, 16, v22
	v_and_b32_e32 v21, 0xffff0000, v22
	v_pk_fma_f32 v[24:25], v[100:101], s[46:47], v[24:25] op_sel_hi:[1,0,1]
	v_lshlrev_b32_e32 v22, 16, v23
	v_and_b32_e32 v23, 0xffff0000, v23
	v_pk_fma_f32 v[30:31], v[96:97], s[46:47], v[20:21] op_sel_hi:[1,0,1]
	v_cvt_pk_bf16_f32 v20, v24, v25
	v_cvt_pk_bf16_f32 v21, v26, v27
	v_pk_fma_f32 v[28:29], v[98:99], s[46:47], v[22:23] op_sel_hi:[1,0,1]
	v_cvt_pk_bf16_f32 v22, v30, v31
	v_pk_mul_f32 v[12:13], v[12:13], v[24:25]
	v_cvt_pk_bf16_f32 v23, v28, v29
	global_store_dwordx4 v[34:35], v[20:23], off
	v_pk_mul_f32 v[10:11], v[10:11], v[28:29]
	s_nop 0
	v_pk_mul_f32 v[20:21], v[8:9], v[30:31]
	v_mov_b32_e32 v8, v203
	v_cvt_pk_fp8_f32 v8, v12, v13
	v_mov_b32_e32 v9, v203
	v_cvt_pk_fp8_f32 v9, v20, v21
	v_pk_mul_f32 v[12:13], v[14:15], v[26:27]
	v_lshlrev_b32_e32 v14, 16, v19
	v_cvt_pk_fp8_f32 v8, v12, v13 op_sel:[0,0,1]
	v_lshlrev_b32_e32 v12, 16, v17
	v_and_b32_e32 v13, 0xffff0000, v17
	v_cvt_pk_fp8_f32 v9, v10, v11 op_sel:[0,0,1]
	v_lshlrev_b32_e32 v10, 16, v16
	v_and_b32_e32 v11, 0xffff0000, v16
	v_pk_fma_f32 v[16:17], v[70:71], s[46:47], v[12:13] op_sel_hi:[1,0,1]
	v_lshlrev_b32_e32 v12, 16, v18
	v_and_b32_e32 v13, 0xffff0000, v18
	v_pk_fma_f32 v[10:11], v[68:69], s[46:47], v[10:11] op_sel_hi:[1,0,1]
	v_pk_fma_f32 v[20:21], v[64:65], s[46:47], v[12:13] op_sel_hi:[1,0,1]
	v_cvt_pk_bf16_f32 v12, v10, v11
	v_pk_mul_f32 v[4:5], v[4:5], v[10:11]
	v_pk_mul_f32 v[0:1], v[0:1], v[20:21]
	v_mov_b32_e32 v10, v203
	v_mov_b32_e32 v11, v203
	v_cvt_pk_fp8_f32 v10, v4, v5
	v_cvt_pk_fp8_f32 v11, v0, v1
	v_and_b32_e32 v15, 0xffff0000, v19
	v_pk_fma_f32 v[18:19], v[66:67], s[46:47], v[14:15] op_sel_hi:[1,0,1]
	v_pk_mul_f32 v[0:1], v[6:7], v[16:17]
	v_pk_mul_f32 v[2:3], v[2:3], v[18:19]
	v_cvt_pk_fp8_f32 v10, v0, v1 op_sel:[0,0,1]
	v_cvt_pk_fp8_f32 v11, v2, v3 op_sel:[0,0,1]
	v_lshl_add_u64 v[0:1], s[42:43], 0, v[36:37]
	v_lshl_add_u64 v[0:1], v[0:1], 0, v[32:33]
	v_cvt_pk_bf16_f32 v13, v16, v17
	v_cvt_pk_bf16_f32 v14, v20, v21
	v_cvt_pk_bf16_f32 v15, v18, v19
	global_store_dwordx4 v[34:35], v[12:15], off offset:16
	global_store_dwordx4 v[0:1], v[8:11], off
	s_and_b64 vcc, exec, s[0:1]
	s_mov_b64 s[0:1], -1
	s_cbranch_vccnz .LBB0_908
	v_readlane_b32 s0, v249, 8
	v_readlane_b32 s1, v249, 9
	s_andn2_b64 vcc, exec, s[0:1]
	s_cbranch_vccnz .LBB0_907
	s_barrier
	s_branch .LBB0_907
	s_nop 0
